# adds: P10 within-block slot ranks computed data-parallel by the 128 assignment threads (32 broadcast ds_read_b128 + compares) instead of 128 serial LDS round trips on 32 threads
# speedup vs baseline: 1.0038x; 1.0029x over previous
.LBB0_1170:
.LBB0_1188:
	s_or_b64 exec, exec, s[24:25]
	s_waitcnt lgkmcnt(0)
	s_barrier
	s_and_saveexec_b64 s[12:13], vcc
	s_cbranch_execz .LBB0_1190
	v_ashrrev_i32_e32 v3, 31, v2
	v_lshlrev_b64 v[2:3], 2, v[2:3]
	v_lshl_add_u64 v[4:5], s[16:17], 0, v[2:3]
	global_load_dword v6, v[4:5], off
	ds_read_b32 v181, v147 offset:4224
	v_mov_b32_e32 v184, 0
	v_mov_b32_e32 v182, 0
	s_mov_b32 s41, 0
	ds_read_b128 v[220:223], v184 offset:4224
	ds_read_b128 v[224:227], v184 offset:4240
	ds_read_b128 v[228:231], v184 offset:4256
	ds_read_b128 v[232:235], v184 offset:4272
	ds_read_b128 v[188:191], v184 offset:4288
	ds_read_b128 v[240:243], v184 offset:4304
	ds_read_b128 v[244:247], v184 offset:4320
	ds_read_b128 v[248:251], v184 offset:4336
	s_waitcnt lgkmcnt(7)
	v_cmp_eq_u32_e64 s[26:27], v220, v181
	v_cmp_lt_u32_e64 s[28:29], s41, v0
	s_and_b64 s[26:27], s[26:27], s[28:29]
	s_add_i32 s41, s41, 1
	v_addc_co_u32_e64 v182, s[30:31], 0, v182, s[26:27]
	v_cmp_eq_u32_e64 s[26:27], v221, v181
	v_cmp_lt_u32_e64 s[28:29], s41, v0
	s_and_b64 s[26:27], s[26:27], s[28:29]
	s_add_i32 s41, s41, 1
	v_addc_co_u32_e64 v182, s[30:31], 0, v182, s[26:27]
	v_cmp_eq_u32_e64 s[26:27], v222, v181
	v_cmp_lt_u32_e64 s[28:29], s41, v0
	s_and_b64 s[26:27], s[26:27], s[28:29]
	s_add_i32 s41, s41, 1
	v_addc_co_u32_e64 v182, s[30:31], 0, v182, s[26:27]
	v_cmp_eq_u32_e64 s[26:27], v223, v181
	v_cmp_lt_u32_e64 s[28:29], s41, v0
	s_and_b64 s[26:27], s[26:27], s[28:29]
	s_add_i32 s41, s41, 1
	v_addc_co_u32_e64 v182, s[30:31], 0, v182, s[26:27]
	s_waitcnt lgkmcnt(6)
	v_cmp_eq_u32_e64 s[26:27], v224, v181
	v_cmp_lt_u32_e64 s[28:29], s41, v0
	s_and_b64 s[26:27], s[26:27], s[28:29]
	s_add_i32 s41, s41, 1
	v_addc_co_u32_e64 v182, s[30:31], 0, v182, s[26:27]
	v_cmp_eq_u32_e64 s[26:27], v225, v181
	v_cmp_lt_u32_e64 s[28:29], s41, v0
	s_and_b64 s[26:27], s[26:27], s[28:29]
	s_add_i32 s41, s41, 1
	v_addc_co_u32_e64 v182, s[30:31], 0, v182, s[26:27]
	v_cmp_eq_u32_e64 s[26:27], v226, v181
	v_cmp_lt_u32_e64 s[28:29], s41, v0
	s_and_b64 s[26:27], s[26:27], s[28:29]
	s_add_i32 s41, s41, 1
	v_addc_co_u32_e64 v182, s[30:31], 0, v182, s[26:27]
	v_cmp_eq_u32_e64 s[26:27], v227, v181
	v_cmp_lt_u32_e64 s[28:29], s41, v0
	s_and_b64 s[26:27], s[26:27], s[28:29]
	s_add_i32 s41, s41, 1
	v_addc_co_u32_e64 v182, s[30:31], 0, v182, s[26:27]
	s_waitcnt lgkmcnt(5)
	v_cmp_eq_u32_e64 s[26:27], v228, v181
	v_cmp_lt_u32_e64 s[28:29], s41, v0
	s_and_b64 s[26:27], s[26:27], s[28:29]
	s_add_i32 s41, s41, 1
	v_addc_co_u32_e64 v182, s[30:31], 0, v182, s[26:27]
	v_cmp_eq_u32_e64 s[26:27], v229, v181
	v_cmp_lt_u32_e64 s[28:29], s41, v0
	s_and_b64 s[26:27], s[26:27], s[28:29]
	s_add_i32 s41, s41, 1
	v_addc_co_u32_e64 v182, s[30:31], 0, v182, s[26:27]
	v_cmp_eq_u32_e64 s[26:27], v230, v181
	v_cmp_lt_u32_e64 s[28:29], s41, v0
	s_and_b64 s[26:27], s[26:27], s[28:29]
	s_add_i32 s41, s41, 1
	v_addc_co_u32_e64 v182, s[30:31], 0, v182, s[26:27]
	v_cmp_eq_u32_e64 s[26:27], v231, v181
	v_cmp_lt_u32_e64 s[28:29], s41, v0
	s_and_b64 s[26:27], s[26:27], s[28:29]
	s_add_i32 s41, s41, 1
	v_addc_co_u32_e64 v182, s[30:31], 0, v182, s[26:27]
	s_waitcnt lgkmcnt(4)
	v_cmp_eq_u32_e64 s[26:27], v232, v181
	v_cmp_lt_u32_e64 s[28:29], s41, v0
	s_and_b64 s[26:27], s[26:27], s[28:29]
	s_add_i32 s41, s41, 1
	v_addc_co_u32_e64 v182, s[30:31], 0, v182, s[26:27]
	v_cmp_eq_u32_e64 s[26:27], v233, v181
	v_cmp_lt_u32_e64 s[28:29], s41, v0
	s_and_b64 s[26:27], s[26:27], s[28:29]
	s_add_i32 s41, s41, 1
	v_addc_co_u32_e64 v182, s[30:31], 0, v182, s[26:27]
	v_cmp_eq_u32_e64 s[26:27], v234, v181
	v_cmp_lt_u32_e64 s[28:29], s41, v0
	s_and_b64 s[26:27], s[26:27], s[28:29]
	s_add_i32 s41, s41, 1
	v_addc_co_u32_e64 v182, s[30:31], 0, v182, s[26:27]
	v_cmp_eq_u32_e64 s[26:27], v235, v181
	v_cmp_lt_u32_e64 s[28:29], s41, v0
	s_and_b64 s[26:27], s[26:27], s[28:29]
	s_add_i32 s41, s41, 1
	v_addc_co_u32_e64 v182, s[30:31], 0, v182, s[26:27]
	s_waitcnt lgkmcnt(3)
	v_cmp_eq_u32_e64 s[26:27], v188, v181
	v_cmp_lt_u32_e64 s[28:29], s41, v0
	s_and_b64 s[26:27], s[26:27], s[28:29]
	s_add_i32 s41, s41, 1
	v_addc_co_u32_e64 v182, s[30:31], 0, v182, s[26:27]
	v_cmp_eq_u32_e64 s[26:27], v189, v181
	v_cmp_lt_u32_e64 s[28:29], s41, v0
	s_and_b64 s[26:27], s[26:27], s[28:29]
	s_add_i32 s41, s41, 1
	v_addc_co_u32_e64 v182, s[30:31], 0, v182, s[26:27]
	v_cmp_eq_u32_e64 s[26:27], v190, v181
	v_cmp_lt_u32_e64 s[28:29], s41, v0
	s_and_b64 s[26:27], s[26:27], s[28:29]
	s_add_i32 s41, s41, 1
	v_addc_co_u32_e64 v182, s[30:31], 0, v182, s[26:27]
	v_cmp_eq_u32_e64 s[26:27], v191, v181
	v_cmp_lt_u32_e64 s[28:29], s41, v0
	s_and_b64 s[26:27], s[26:27], s[28:29]
	s_add_i32 s41, s41, 1
	v_addc_co_u32_e64 v182, s[30:31], 0, v182, s[26:27]
	s_waitcnt lgkmcnt(2)
	v_cmp_eq_u32_e64 s[26:27], v240, v181
	v_cmp_lt_u32_e64 s[28:29], s41, v0
	s_and_b64 s[26:27], s[26:27], s[28:29]
	s_add_i32 s41, s41, 1
	v_addc_co_u32_e64 v182, s[30:31], 0, v182, s[26:27]
	v_cmp_eq_u32_e64 s[26:27], v241, v181
	v_cmp_lt_u32_e64 s[28:29], s41, v0
	s_and_b64 s[26:27], s[26:27], s[28:29]
	s_add_i32 s41, s41, 1
	v_addc_co_u32_e64 v182, s[30:31], 0, v182, s[26:27]
	v_cmp_eq_u32_e64 s[26:27], v242, v181
	v_cmp_lt_u32_e64 s[28:29], s41, v0
	s_and_b64 s[26:27], s[26:27], s[28:29]
	s_add_i32 s41, s41, 1
	v_addc_co_u32_e64 v182, s[30:31], 0, v182, s[26:27]
	v_cmp_eq_u32_e64 s[26:27], v243, v181
	v_cmp_lt_u32_e64 s[28:29], s41, v0
	s_and_b64 s[26:27], s[26:27], s[28:29]
	s_add_i32 s41, s41, 1
	v_addc_co_u32_e64 v182, s[30:31], 0, v182, s[26:27]
	s_waitcnt lgkmcnt(1)
	v_cmp_eq_u32_e64 s[26:27], v244, v181
	v_cmp_lt_u32_e64 s[28:29], s41, v0
	s_and_b64 s[26:27], s[26:27], s[28:29]
	s_add_i32 s41, s41, 1
	v_addc_co_u32_e64 v182, s[30:31], 0, v182, s[26:27]
	v_cmp_eq_u32_e64 s[26:27], v245, v181
	v_cmp_lt_u32_e64 s[28:29], s41, v0
	s_and_b64 s[26:27], s[26:27], s[28:29]
	s_add_i32 s41, s41, 1
	v_addc_co_u32_e64 v182, s[30:31], 0, v182, s[26:27]
	v_cmp_eq_u32_e64 s[26:27], v246, v181
	v_cmp_lt_u32_e64 s[28:29], s41, v0
	s_and_b64 s[26:27], s[26:27], s[28:29]
	s_add_i32 s41, s41, 1
	v_addc_co_u32_e64 v182, s[30:31], 0, v182, s[26:27]
	v_cmp_eq_u32_e64 s[26:27], v247, v181
	v_cmp_lt_u32_e64 s[28:29], s41, v0
	s_and_b64 s[26:27], s[26:27], s[28:29]
	s_add_i32 s41, s41, 1
	v_addc_co_u32_e64 v182, s[30:31], 0, v182, s[26:27]
	s_waitcnt lgkmcnt(0)
	v_cmp_eq_u32_e64 s[26:27], v248, v181
	v_cmp_lt_u32_e64 s[28:29], s41, v0
	s_and_b64 s[26:27], s[26:27], s[28:29]
	s_add_i32 s41, s41, 1
	v_addc_co_u32_e64 v182, s[30:31], 0, v182, s[26:27]
	v_cmp_eq_u32_e64 s[26:27], v249, v181
	v_cmp_lt_u32_e64 s[28:29], s41, v0
	s_and_b64 s[26:27], s[26:27], s[28:29]
	s_add_i32 s41, s41, 1
	v_addc_co_u32_e64 v182, s[30:31], 0, v182, s[26:27]
	v_cmp_eq_u32_e64 s[26:27], v250, v181
	v_cmp_lt_u32_e64 s[28:29], s41, v0
	s_and_b64 s[26:27], s[26:27], s[28:29]
	s_add_i32 s41, s41, 1
	v_addc_co_u32_e64 v182, s[30:31], 0, v182, s[26:27]
	v_cmp_eq_u32_e64 s[26:27], v251, v181
	v_cmp_lt_u32_e64 s[28:29], s41, v0
	s_and_b64 s[26:27], s[26:27], s[28:29]
	s_add_i32 s41, s41, 1
	v_addc_co_u32_e64 v182, s[30:31], 0, v182, s[26:27]
	ds_read_b128 v[220:223], v184 offset:4352
	ds_read_b128 v[224:227], v184 offset:4368
	ds_read_b128 v[228:231], v184 offset:4384
	ds_read_b128 v[232:235], v184 offset:4400
	ds_read_b128 v[188:191], v184 offset:4416
	ds_read_b128 v[240:243], v184 offset:4432
	ds_read_b128 v[244:247], v184 offset:4448
	ds_read_b128 v[248:251], v184 offset:4464
	s_waitcnt lgkmcnt(7)
	v_cmp_eq_u32_e64 s[26:27], v220, v181
	v_cmp_lt_u32_e64 s[28:29], s41, v0
	s_and_b64 s[26:27], s[26:27], s[28:29]
	s_add_i32 s41, s41, 1
	v_addc_co_u32_e64 v182, s[30:31], 0, v182, s[26:27]
	v_cmp_eq_u32_e64 s[26:27], v221, v181
	v_cmp_lt_u32_e64 s[28:29], s41, v0
	s_and_b64 s[26:27], s[26:27], s[28:29]
	s_add_i32 s41, s41, 1
	v_addc_co_u32_e64 v182, s[30:31], 0, v182, s[26:27]
	v_cmp_eq_u32_e64 s[26:27], v222, v181
	v_cmp_lt_u32_e64 s[28:29], s41, v0
	s_and_b64 s[26:27], s[26:27], s[28:29]
	s_add_i32 s41, s41, 1
	v_addc_co_u32_e64 v182, s[30:31], 0, v182, s[26:27]
	v_cmp_eq_u32_e64 s[26:27], v223, v181
	v_cmp_lt_u32_e64 s[28:29], s41, v0
	s_and_b64 s[26:27], s[26:27], s[28:29]
	s_add_i32 s41, s41, 1
	v_addc_co_u32_e64 v182, s[30:31], 0, v182, s[26:27]
	s_waitcnt lgkmcnt(6)
	v_cmp_eq_u32_e64 s[26:27], v224, v181
	v_cmp_lt_u32_e64 s[28:29], s41, v0
	s_and_b64 s[26:27], s[26:27], s[28:29]
	s_add_i32 s41, s41, 1
	v_addc_co_u32_e64 v182, s[30:31], 0, v182, s[26:27]
	v_cmp_eq_u32_e64 s[26:27], v225, v181
	v_cmp_lt_u32_e64 s[28:29], s41, v0
	s_and_b64 s[26:27], s[26:27], s[28:29]
	s_add_i32 s41, s41, 1
	v_addc_co_u32_e64 v182, s[30:31], 0, v182, s[26:27]
	v_cmp_eq_u32_e64 s[26:27], v226, v181
	v_cmp_lt_u32_e64 s[28:29], s41, v0
	s_and_b64 s[26:27], s[26:27], s[28:29]
	s_add_i32 s41, s41, 1
	v_addc_co_u32_e64 v182, s[30:31], 0, v182, s[26:27]
	v_cmp_eq_u32_e64 s[26:27], v227, v181
	v_cmp_lt_u32_e64 s[28:29], s41, v0
	s_and_b64 s[26:27], s[26:27], s[28:29]
	s_add_i32 s41, s41, 1
	v_addc_co_u32_e64 v182, s[30:31], 0, v182, s[26:27]
	s_waitcnt lgkmcnt(5)
	v_cmp_eq_u32_e64 s[26:27], v228, v181
	v_cmp_lt_u32_e64 s[28:29], s41, v0
	s_and_b64 s[26:27], s[26:27], s[28:29]
	s_add_i32 s41, s41, 1
	v_addc_co_u32_e64 v182, s[30:31], 0, v182, s[26:27]
	v_cmp_eq_u32_e64 s[26:27], v229, v181
	v_cmp_lt_u32_e64 s[28:29], s41, v0
	s_and_b64 s[26:27], s[26:27], s[28:29]
	s_add_i32 s41, s41, 1
	v_addc_co_u32_e64 v182, s[30:31], 0, v182, s[26:27]
	v_cmp_eq_u32_e64 s[26:27], v230, v181
	v_cmp_lt_u32_e64 s[28:29], s41, v0
	s_and_b64 s[26:27], s[26:27], s[28:29]
	s_add_i32 s41, s41, 1
	v_addc_co_u32_e64 v182, s[30:31], 0, v182, s[26:27]
	v_cmp_eq_u32_e64 s[26:27], v231, v181
	v_cmp_lt_u32_e64 s[28:29], s41, v0
	s_and_b64 s[26:27], s[26:27], s[28:29]
	s_add_i32 s41, s41, 1
	v_addc_co_u32_e64 v182, s[30:31], 0, v182, s[26:27]
	s_waitcnt lgkmcnt(4)
	v_cmp_eq_u32_e64 s[26:27], v232, v181
	v_cmp_lt_u32_e64 s[28:29], s41, v0
	s_and_b64 s[26:27], s[26:27], s[28:29]
	s_add_i32 s41, s41, 1
	v_addc_co_u32_e64 v182, s[30:31], 0, v182, s[26:27]
	v_cmp_eq_u32_e64 s[26:27], v233, v181
	v_cmp_lt_u32_e64 s[28:29], s41, v0
	s_and_b64 s[26:27], s[26:27], s[28:29]
	s_add_i32 s41, s41, 1
	v_addc_co_u32_e64 v182, s[30:31], 0, v182, s[26:27]
	v_cmp_eq_u32_e64 s[26:27], v234, v181
	v_cmp_lt_u32_e64 s[28:29], s41, v0
	s_and_b64 s[26:27], s[26:27], s[28:29]
	s_add_i32 s41, s41, 1
	v_addc_co_u32_e64 v182, s[30:31], 0, v182, s[26:27]
	v_cmp_eq_u32_e64 s[26:27], v235, v181
	v_cmp_lt_u32_e64 s[28:29], s41, v0
	s_and_b64 s[26:27], s[26:27], s[28:29]
	s_add_i32 s41, s41, 1
	v_addc_co_u32_e64 v182, s[30:31], 0, v182, s[26:27]
	s_waitcnt lgkmcnt(3)
	v_cmp_eq_u32_e64 s[26:27], v188, v181
	v_cmp_lt_u32_e64 s[28:29], s41, v0
	s_and_b64 s[26:27], s[26:27], s[28:29]
	s_add_i32 s41, s41, 1
	v_addc_co_u32_e64 v182, s[30:31], 0, v182, s[26:27]
	v_cmp_eq_u32_e64 s[26:27], v189, v181
	v_cmp_lt_u32_e64 s[28:29], s41, v0
	s_and_b64 s[26:27], s[26:27], s[28:29]
	s_add_i32 s41, s41, 1
	v_addc_co_u32_e64 v182, s[30:31], 0, v182, s[26:27]
	v_cmp_eq_u32_e64 s[26:27], v190, v181
	v_cmp_lt_u32_e64 s[28:29], s41, v0
	s_and_b64 s[26:27], s[26:27], s[28:29]
	s_add_i32 s41, s41, 1
	v_addc_co_u32_e64 v182, s[30:31], 0, v182, s[26:27]
	v_cmp_eq_u32_e64 s[26:27], v191, v181
	v_cmp_lt_u32_e64 s[28:29], s41, v0
	s_and_b64 s[26:27], s[26:27], s[28:29]
	s_add_i32 s41, s41, 1
	v_addc_co_u32_e64 v182, s[30:31], 0, v182, s[26:27]
	s_waitcnt lgkmcnt(2)
	v_cmp_eq_u32_e64 s[26:27], v240, v181
	v_cmp_lt_u32_e64 s[28:29], s41, v0
	s_and_b64 s[26:27], s[26:27], s[28:29]
	s_add_i32 s41, s41, 1
	v_addc_co_u32_e64 v182, s[30:31], 0, v182, s[26:27]
	v_cmp_eq_u32_e64 s[26:27], v241, v181
	v_cmp_lt_u32_e64 s[28:29], s41, v0
	s_and_b64 s[26:27], s[26:27], s[28:29]
	s_add_i32 s41, s41, 1
	v_addc_co_u32_e64 v182, s[30:31], 0, v182, s[26:27]
	v_cmp_eq_u32_e64 s[26:27], v242, v181
	v_cmp_lt_u32_e64 s[28:29], s41, v0
	s_and_b64 s[26:27], s[26:27], s[28:29]
	s_add_i32 s41, s41, 1
	v_addc_co_u32_e64 v182, s[30:31], 0, v182, s[26:27]
	v_cmp_eq_u32_e64 s[26:27], v243, v181
	v_cmp_lt_u32_e64 s[28:29], s41, v0
	s_and_b64 s[26:27], s[26:27], s[28:29]
	s_add_i32 s41, s41, 1
	v_addc_co_u32_e64 v182, s[30:31], 0, v182, s[26:27]
	s_waitcnt lgkmcnt(1)
	v_cmp_eq_u32_e64 s[26:27], v244, v181
	v_cmp_lt_u32_e64 s[28:29], s41, v0
	s_and_b64 s[26:27], s[26:27], s[28:29]
	s_add_i32 s41, s41, 1
	v_addc_co_u32_e64 v182, s[30:31], 0, v182, s[26:27]
	v_cmp_eq_u32_e64 s[26:27], v245, v181
	v_cmp_lt_u32_e64 s[28:29], s41, v0
	s_and_b64 s[26:27], s[26:27], s[28:29]
	s_add_i32 s41, s41, 1
	v_addc_co_u32_e64 v182, s[30:31], 0, v182, s[26:27]
	v_cmp_eq_u32_e64 s[26:27], v246, v181
	v_cmp_lt_u32_e64 s[28:29], s41, v0
	s_and_b64 s[26:27], s[26:27], s[28:29]
	s_add_i32 s41, s41, 1
	v_addc_co_u32_e64 v182, s[30:31], 0, v182, s[26:27]
	v_cmp_eq_u32_e64 s[26:27], v247, v181
	v_cmp_lt_u32_e64 s[28:29], s41, v0
	s_and_b64 s[26:27], s[26:27], s[28:29]
	s_add_i32 s41, s41, 1
	v_addc_co_u32_e64 v182, s[30:31], 0, v182, s[26:27]
	s_waitcnt lgkmcnt(0)
	v_cmp_eq_u32_e64 s[26:27], v248, v181
	v_cmp_lt_u32_e64 s[28:29], s41, v0
	s_and_b64 s[26:27], s[26:27], s[28:29]
	s_add_i32 s41, s41, 1
	v_addc_co_u32_e64 v182, s[30:31], 0, v182, s[26:27]
	v_cmp_eq_u32_e64 s[26:27], v249, v181
	v_cmp_lt_u32_e64 s[28:29], s41, v0
	s_and_b64 s[26:27], s[26:27], s[28:29]
	s_add_i32 s41, s41, 1
	v_addc_co_u32_e64 v182, s[30:31], 0, v182, s[26:27]
	v_cmp_eq_u32_e64 s[26:27], v250, v181
	v_cmp_lt_u32_e64 s[28:29], s41, v0
	s_and_b64 s[26:27], s[26:27], s[28:29]
	s_add_i32 s41, s41, 1
	v_addc_co_u32_e64 v182, s[30:31], 0, v182, s[26:27]
	v_cmp_eq_u32_e64 s[26:27], v251, v181
	v_cmp_lt_u32_e64 s[28:29], s41, v0
	s_and_b64 s[26:27], s[26:27], s[28:29]
	s_add_i32 s41, s41, 1
	v_addc_co_u32_e64 v182, s[30:31], 0, v182, s[26:27]
	ds_read_b128 v[220:223], v184 offset:4480
	ds_read_b128 v[224:227], v184 offset:4496
	ds_read_b128 v[228:231], v184 offset:4512
	ds_read_b128 v[232:235], v184 offset:4528
	ds_read_b128 v[188:191], v184 offset:4544
	ds_read_b128 v[240:243], v184 offset:4560
	ds_read_b128 v[244:247], v184 offset:4576
	ds_read_b128 v[248:251], v184 offset:4592
	s_waitcnt lgkmcnt(7)
	v_cmp_eq_u32_e64 s[26:27], v220, v181
	v_cmp_lt_u32_e64 s[28:29], s41, v0
	s_and_b64 s[26:27], s[26:27], s[28:29]
	s_add_i32 s41, s41, 1
	v_addc_co_u32_e64 v182, s[30:31], 0, v182, s[26:27]
	v_cmp_eq_u32_e64 s[26:27], v221, v181
	v_cmp_lt_u32_e64 s[28:29], s41, v0
	s_and_b64 s[26:27], s[26:27], s[28:29]
	s_add_i32 s41, s41, 1
	v_addc_co_u32_e64 v182, s[30:31], 0, v182, s[26:27]
	v_cmp_eq_u32_e64 s[26:27], v222, v181
	v_cmp_lt_u32_e64 s[28:29], s41, v0
	s_and_b64 s[26:27], s[26:27], s[28:29]
	s_add_i32 s41, s41, 1
	v_addc_co_u32_e64 v182, s[30:31], 0, v182, s[26:27]
	v_cmp_eq_u32_e64 s[26:27], v223, v181
	v_cmp_lt_u32_e64 s[28:29], s41, v0
	s_and_b64 s[26:27], s[26:27], s[28:29]
	s_add_i32 s41, s41, 1
	v_addc_co_u32_e64 v182, s[30:31], 0, v182, s[26:27]
	s_waitcnt lgkmcnt(6)
	v_cmp_eq_u32_e64 s[26:27], v224, v181
	v_cmp_lt_u32_e64 s[28:29], s41, v0
	s_and_b64 s[26:27], s[26:27], s[28:29]
	s_add_i32 s41, s41, 1
	v_addc_co_u32_e64 v182, s[30:31], 0, v182, s[26:27]
	v_cmp_eq_u32_e64 s[26:27], v225, v181
	v_cmp_lt_u32_e64 s[28:29], s41, v0
	s_and_b64 s[26:27], s[26:27], s[28:29]
	s_add_i32 s41, s41, 1
	v_addc_co_u32_e64 v182, s[30:31], 0, v182, s[26:27]
	v_cmp_eq_u32_e64 s[26:27], v226, v181
	v_cmp_lt_u32_e64 s[28:29], s41, v0
	s_and_b64 s[26:27], s[26:27], s[28:29]
	s_add_i32 s41, s41, 1
	v_addc_co_u32_e64 v182, s[30:31], 0, v182, s[26:27]
	v_cmp_eq_u32_e64 s[26:27], v227, v181
	v_cmp_lt_u32_e64 s[28:29], s41, v0
	s_and_b64 s[26:27], s[26:27], s[28:29]
	s_add_i32 s41, s41, 1
	v_addc_co_u32_e64 v182, s[30:31], 0, v182, s[26:27]
	s_waitcnt lgkmcnt(5)
	v_cmp_eq_u32_e64 s[26:27], v228, v181
	v_cmp_lt_u32_e64 s[28:29], s41, v0
	s_and_b64 s[26:27], s[26:27], s[28:29]
	s_add_i32 s41, s41, 1
	v_addc_co_u32_e64 v182, s[30:31], 0, v182, s[26:27]
	v_cmp_eq_u32_e64 s[26:27], v229, v181
	v_cmp_lt_u32_e64 s[28:29], s41, v0
	s_and_b64 s[26:27], s[26:27], s[28:29]
	s_add_i32 s41, s41, 1
	v_addc_co_u32_e64 v182, s[30:31], 0, v182, s[26:27]
	v_cmp_eq_u32_e64 s[26:27], v230, v181
	v_cmp_lt_u32_e64 s[28:29], s41, v0
	s_and_b64 s[26:27], s[26:27], s[28:29]
	s_add_i32 s41, s41, 1
	v_addc_co_u32_e64 v182, s[30:31], 0, v182, s[26:27]
	v_cmp_eq_u32_e64 s[26:27], v231, v181
	v_cmp_lt_u32_e64 s[28:29], s41, v0
	s_and_b64 s[26:27], s[26:27], s[28:29]
	s_add_i32 s41, s41, 1
	v_addc_co_u32_e64 v182, s[30:31], 0, v182, s[26:27]
	s_waitcnt lgkmcnt(4)
	v_cmp_eq_u32_e64 s[26:27], v232, v181
	v_cmp_lt_u32_e64 s[28:29], s41, v0
	s_and_b64 s[26:27], s[26:27], s[28:29]
	s_add_i32 s41, s41, 1
	v_addc_co_u32_e64 v182, s[30:31], 0, v182, s[26:27]
	v_cmp_eq_u32_e64 s[26:27], v233, v181
	v_cmp_lt_u32_e64 s[28:29], s41, v0
	s_and_b64 s[26:27], s[26:27], s[28:29]
	s_add_i32 s41, s41, 1
	v_addc_co_u32_e64 v182, s[30:31], 0, v182, s[26:27]
	v_cmp_eq_u32_e64 s[26:27], v234, v181
	v_cmp_lt_u32_e64 s[28:29], s41, v0
	s_and_b64 s[26:27], s[26:27], s[28:29]
	s_add_i32 s41, s41, 1
	v_addc_co_u32_e64 v182, s[30:31], 0, v182, s[26:27]
	v_cmp_eq_u32_e64 s[26:27], v235, v181
	v_cmp_lt_u32_e64 s[28:29], s41, v0
	s_and_b64 s[26:27], s[26:27], s[28:29]
	s_add_i32 s41, s41, 1
	v_addc_co_u32_e64 v182, s[30:31], 0, v182, s[26:27]
	s_waitcnt lgkmcnt(3)
	v_cmp_eq_u32_e64 s[26:27], v188, v181
	v_cmp_lt_u32_e64 s[28:29], s41, v0
	s_and_b64 s[26:27], s[26:27], s[28:29]
	s_add_i32 s41, s41, 1
	v_addc_co_u32_e64 v182, s[30:31], 0, v182, s[26:27]
	v_cmp_eq_u32_e64 s[26:27], v189, v181
	v_cmp_lt_u32_e64 s[28:29], s41, v0
	s_and_b64 s[26:27], s[26:27], s[28:29]
	s_add_i32 s41, s41, 1
	v_addc_co_u32_e64 v182, s[30:31], 0, v182, s[26:27]
	v_cmp_eq_u32_e64 s[26:27], v190, v181
	v_cmp_lt_u32_e64 s[28:29], s41, v0
	s_and_b64 s[26:27], s[26:27], s[28:29]
	s_add_i32 s41, s41, 1
	v_addc_co_u32_e64 v182, s[30:31], 0, v182, s[26:27]
	v_cmp_eq_u32_e64 s[26:27], v191, v181
	v_cmp_lt_u32_e64 s[28:29], s41, v0
	s_and_b64 s[26:27], s[26:27], s[28:29]
	s_add_i32 s41, s41, 1
	v_addc_co_u32_e64 v182, s[30:31], 0, v182, s[26:27]
	s_waitcnt lgkmcnt(2)
	v_cmp_eq_u32_e64 s[26:27], v240, v181
	v_cmp_lt_u32_e64 s[28:29], s41, v0
	s_and_b64 s[26:27], s[26:27], s[28:29]
	s_add_i32 s41, s41, 1
	v_addc_co_u32_e64 v182, s[30:31], 0, v182, s[26:27]
	v_cmp_eq_u32_e64 s[26:27], v241, v181
	v_cmp_lt_u32_e64 s[28:29], s41, v0
	s_and_b64 s[26:27], s[26:27], s[28:29]
	s_add_i32 s41, s41, 1
	v_addc_co_u32_e64 v182, s[30:31], 0, v182, s[26:27]
	v_cmp_eq_u32_e64 s[26:27], v242, v181
	v_cmp_lt_u32_e64 s[28:29], s41, v0
	s_and_b64 s[26:27], s[26:27], s[28:29]
	s_add_i32 s41, s41, 1
	v_addc_co_u32_e64 v182, s[30:31], 0, v182, s[26:27]
	v_cmp_eq_u32_e64 s[26:27], v243, v181
	v_cmp_lt_u32_e64 s[28:29], s41, v0
	s_and_b64 s[26:27], s[26:27], s[28:29]
	s_add_i32 s41, s41, 1
	v_addc_co_u32_e64 v182, s[30:31], 0, v182, s[26:27]
	s_waitcnt lgkmcnt(1)
	v_cmp_eq_u32_e64 s[26:27], v244, v181
	v_cmp_lt_u32_e64 s[28:29], s41, v0
	s_and_b64 s[26:27], s[26:27], s[28:29]
	s_add_i32 s41, s41, 1
	v_addc_co_u32_e64 v182, s[30:31], 0, v182, s[26:27]
	v_cmp_eq_u32_e64 s[26:27], v245, v181
	v_cmp_lt_u32_e64 s[28:29], s41, v0
	s_and_b64 s[26:27], s[26:27], s[28:29]
	s_add_i32 s41, s41, 1
	v_addc_co_u32_e64 v182, s[30:31], 0, v182, s[26:27]
	v_cmp_eq_u32_e64 s[26:27], v246, v181
	v_cmp_lt_u32_e64 s[28:29], s41, v0
	s_and_b64 s[26:27], s[26:27], s[28:29]
	s_add_i32 s41, s41, 1
	v_addc_co_u32_e64 v182, s[30:31], 0, v182, s[26:27]
	v_cmp_eq_u32_e64 s[26:27], v247, v181
	v_cmp_lt_u32_e64 s[28:29], s41, v0
	s_and_b64 s[26:27], s[26:27], s[28:29]
	s_add_i32 s41, s41, 1
	v_addc_co_u32_e64 v182, s[30:31], 0, v182, s[26:27]
	s_waitcnt lgkmcnt(0)
	v_cmp_eq_u32_e64 s[26:27], v248, v181
	v_cmp_lt_u32_e64 s[28:29], s41, v0
	s_and_b64 s[26:27], s[26:27], s[28:29]
	s_add_i32 s41, s41, 1
	v_addc_co_u32_e64 v182, s[30:31], 0, v182, s[26:27]
	v_cmp_eq_u32_e64 s[26:27], v249, v181
	v_cmp_lt_u32_e64 s[28:29], s41, v0
	s_and_b64 s[26:27], s[26:27], s[28:29]
	s_add_i32 s41, s41, 1
	v_addc_co_u32_e64 v182, s[30:31], 0, v182, s[26:27]
	v_cmp_eq_u32_e64 s[26:27], v250, v181
	v_cmp_lt_u32_e64 s[28:29], s41, v0
	s_and_b64 s[26:27], s[26:27], s[28:29]
	s_add_i32 s41, s41, 1
	v_addc_co_u32_e64 v182, s[30:31], 0, v182, s[26:27]
	v_cmp_eq_u32_e64 s[26:27], v251, v181
	v_cmp_lt_u32_e64 s[28:29], s41, v0
	s_and_b64 s[26:27], s[26:27], s[28:29]
	s_add_i32 s41, s41, 1
	v_addc_co_u32_e64 v182, s[30:31], 0, v182, s[26:27]
	ds_read_b128 v[220:223], v184 offset:4608
	ds_read_b128 v[224:227], v184 offset:4624
	ds_read_b128 v[228:231], v184 offset:4640
	ds_read_b128 v[232:235], v184 offset:4656
	ds_read_b128 v[188:191], v184 offset:4672
	ds_read_b128 v[240:243], v184 offset:4688
	ds_read_b128 v[244:247], v184 offset:4704
	ds_read_b128 v[248:251], v184 offset:4720
	s_waitcnt lgkmcnt(7)
	v_cmp_eq_u32_e64 s[26:27], v220, v181
	v_cmp_lt_u32_e64 s[28:29], s41, v0
	s_and_b64 s[26:27], s[26:27], s[28:29]
	s_add_i32 s41, s41, 1
	v_addc_co_u32_e64 v182, s[30:31], 0, v182, s[26:27]
	v_cmp_eq_u32_e64 s[26:27], v221, v181
	v_cmp_lt_u32_e64 s[28:29], s41, v0
	s_and_b64 s[26:27], s[26:27], s[28:29]
	s_add_i32 s41, s41, 1
	v_addc_co_u32_e64 v182, s[30:31], 0, v182, s[26:27]
	v_cmp_eq_u32_e64 s[26:27], v222, v181
	v_cmp_lt_u32_e64 s[28:29], s41, v0
	s_and_b64 s[26:27], s[26:27], s[28:29]
	s_add_i32 s41, s41, 1
	v_addc_co_u32_e64 v182, s[30:31], 0, v182, s[26:27]
	v_cmp_eq_u32_e64 s[26:27], v223, v181
	v_cmp_lt_u32_e64 s[28:29], s41, v0
	s_and_b64 s[26:27], s[26:27], s[28:29]
	s_add_i32 s41, s41, 1
	v_addc_co_u32_e64 v182, s[30:31], 0, v182, s[26:27]
	s_waitcnt lgkmcnt(6)
	v_cmp_eq_u32_e64 s[26:27], v224, v181
	v_cmp_lt_u32_e64 s[28:29], s41, v0
	s_and_b64 s[26:27], s[26:27], s[28:29]
	s_add_i32 s41, s41, 1
	v_addc_co_u32_e64 v182, s[30:31], 0, v182, s[26:27]
	v_cmp_eq_u32_e64 s[26:27], v225, v181
	v_cmp_lt_u32_e64 s[28:29], s41, v0
	s_and_b64 s[26:27], s[26:27], s[28:29]
	s_add_i32 s41, s41, 1
	v_addc_co_u32_e64 v182, s[30:31], 0, v182, s[26:27]
	v_cmp_eq_u32_e64 s[26:27], v226, v181
	v_cmp_lt_u32_e64 s[28:29], s41, v0
	s_and_b64 s[26:27], s[26:27], s[28:29]
	s_add_i32 s41, s41, 1
	v_addc_co_u32_e64 v182, s[30:31], 0, v182, s[26:27]
	v_cmp_eq_u32_e64 s[26:27], v227, v181
	v_cmp_lt_u32_e64 s[28:29], s41, v0
	s_and_b64 s[26:27], s[26:27], s[28:29]
	s_add_i32 s41, s41, 1
	v_addc_co_u32_e64 v182, s[30:31], 0, v182, s[26:27]
	s_waitcnt lgkmcnt(5)
	v_cmp_eq_u32_e64 s[26:27], v228, v181
	v_cmp_lt_u32_e64 s[28:29], s41, v0
	s_and_b64 s[26:27], s[26:27], s[28:29]
	s_add_i32 s41, s41, 1
	v_addc_co_u32_e64 v182, s[30:31], 0, v182, s[26:27]
	v_cmp_eq_u32_e64 s[26:27], v229, v181
	v_cmp_lt_u32_e64 s[28:29], s41, v0
	s_and_b64 s[26:27], s[26:27], s[28:29]
	s_add_i32 s41, s41, 1
	v_addc_co_u32_e64 v182, s[30:31], 0, v182, s[26:27]
	v_cmp_eq_u32_e64 s[26:27], v230, v181
	v_cmp_lt_u32_e64 s[28:29], s41, v0
	s_and_b64 s[26:27], s[26:27], s[28:29]
	s_add_i32 s41, s41, 1
	v_addc_co_u32_e64 v182, s[30:31], 0, v182, s[26:27]
	v_cmp_eq_u32_e64 s[26:27], v231, v181
	v_cmp_lt_u32_e64 s[28:29], s41, v0
	s_and_b64 s[26:27], s[26:27], s[28:29]
	s_add_i32 s41, s41, 1
	v_addc_co_u32_e64 v182, s[30:31], 0, v182, s[26:27]
	s_waitcnt lgkmcnt(4)
	v_cmp_eq_u32_e64 s[26:27], v232, v181
	v_cmp_lt_u32_e64 s[28:29], s41, v0
	s_and_b64 s[26:27], s[26:27], s[28:29]
	s_add_i32 s41, s41, 1
	v_addc_co_u32_e64 v182, s[30:31], 0, v182, s[26:27]
	v_cmp_eq_u32_e64 s[26:27], v233, v181
	v_cmp_lt_u32_e64 s[28:29], s41, v0
	s_and_b64 s[26:27], s[26:27], s[28:29]
	s_add_i32 s41, s41, 1
	v_addc_co_u32_e64 v182, s[30:31], 0, v182, s[26:27]
	v_cmp_eq_u32_e64 s[26:27], v234, v181
	v_cmp_lt_u32_e64 s[28:29], s41, v0
	s_and_b64 s[26:27], s[26:27], s[28:29]
	s_add_i32 s41, s41, 1
	v_addc_co_u32_e64 v182, s[30:31], 0, v182, s[26:27]
	v_cmp_eq_u32_e64 s[26:27], v235, v181
	v_cmp_lt_u32_e64 s[28:29], s41, v0
	s_and_b64 s[26:27], s[26:27], s[28:29]
	s_add_i32 s41, s41, 1
	v_addc_co_u32_e64 v182, s[30:31], 0, v182, s[26:27]
	s_waitcnt lgkmcnt(3)
	v_cmp_eq_u32_e64 s[26:27], v188, v181
	v_cmp_lt_u32_e64 s[28:29], s41, v0
	s_and_b64 s[26:27], s[26:27], s[28:29]
	s_add_i32 s41, s41, 1
	v_addc_co_u32_e64 v182, s[30:31], 0, v182, s[26:27]
	v_cmp_eq_u32_e64 s[26:27], v189, v181
	v_cmp_lt_u32_e64 s[28:29], s41, v0
	s_and_b64 s[26:27], s[26:27], s[28:29]
	s_add_i32 s41, s41, 1
	v_addc_co_u32_e64 v182, s[30:31], 0, v182, s[26:27]
	v_cmp_eq_u32_e64 s[26:27], v190, v181
	v_cmp_lt_u32_e64 s[28:29], s41, v0
	s_and_b64 s[26:27], s[26:27], s[28:29]
	s_add_i32 s41, s41, 1
	v_addc_co_u32_e64 v182, s[30:31], 0, v182, s[26:27]
	v_cmp_eq_u32_e64 s[26:27], v191, v181
	v_cmp_lt_u32_e64 s[28:29], s41, v0
	s_and_b64 s[26:27], s[26:27], s[28:29]
	s_add_i32 s41, s41, 1
	v_addc_co_u32_e64 v182, s[30:31], 0, v182, s[26:27]
	s_waitcnt lgkmcnt(2)
	v_cmp_eq_u32_e64 s[26:27], v240, v181
	v_cmp_lt_u32_e64 s[28:29], s41, v0
	s_and_b64 s[26:27], s[26:27], s[28:29]
	s_add_i32 s41, s41, 1
	v_addc_co_u32_e64 v182, s[30:31], 0, v182, s[26:27]
	v_cmp_eq_u32_e64 s[26:27], v241, v181
	v_cmp_lt_u32_e64 s[28:29], s41, v0
	s_and_b64 s[26:27], s[26:27], s[28:29]
	s_add_i32 s41, s41, 1
	v_addc_co_u32_e64 v182, s[30:31], 0, v182, s[26:27]
	v_cmp_eq_u32_e64 s[26:27], v242, v181
	v_cmp_lt_u32_e64 s[28:29], s41, v0
	s_and_b64 s[26:27], s[26:27], s[28:29]
	s_add_i32 s41, s41, 1
	v_addc_co_u32_e64 v182, s[30:31], 0, v182, s[26:27]
	v_cmp_eq_u32_e64 s[26:27], v243, v181
	v_cmp_lt_u32_e64 s[28:29], s41, v0
	s_and_b64 s[26:27], s[26:27], s[28:29]
	s_add_i32 s41, s41, 1
	v_addc_co_u32_e64 v182, s[30:31], 0, v182, s[26:27]
	s_waitcnt lgkmcnt(1)
	v_cmp_eq_u32_e64 s[26:27], v244, v181
	v_cmp_lt_u32_e64 s[28:29], s41, v0
	s_and_b64 s[26:27], s[26:27], s[28:29]
	s_add_i32 s41, s41, 1
	v_addc_co_u32_e64 v182, s[30:31], 0, v182, s[26:27]
	v_cmp_eq_u32_e64 s[26:27], v245, v181
	v_cmp_lt_u32_e64 s[28:29], s41, v0
	s_and_b64 s[26:27], s[26:27], s[28:29]
	s_add_i32 s41, s41, 1
	v_addc_co_u32_e64 v182, s[30:31], 0, v182, s[26:27]
	v_cmp_eq_u32_e64 s[26:27], v246, v181
	v_cmp_lt_u32_e64 s[28:29], s41, v0
	s_and_b64 s[26:27], s[26:27], s[28:29]
	s_add_i32 s41, s41, 1
	v_addc_co_u32_e64 v182, s[30:31], 0, v182, s[26:27]
	v_cmp_eq_u32_e64 s[26:27], v247, v181
	v_cmp_lt_u32_e64 s[28:29], s41, v0
	s_and_b64 s[26:27], s[26:27], s[28:29]
	s_add_i32 s41, s41, 1
	v_addc_co_u32_e64 v182, s[30:31], 0, v182, s[26:27]
	s_waitcnt lgkmcnt(0)
	v_cmp_eq_u32_e64 s[26:27], v248, v181
	v_cmp_lt_u32_e64 s[28:29], s41, v0
	s_and_b64 s[26:27], s[26:27], s[28:29]
	s_add_i32 s41, s41, 1
	v_addc_co_u32_e64 v182, s[30:31], 0, v182, s[26:27]
	v_cmp_eq_u32_e64 s[26:27], v249, v181
	v_cmp_lt_u32_e64 s[28:29], s41, v0
	s_and_b64 s[26:27], s[26:27], s[28:29]
	s_add_i32 s41, s41, 1
	v_addc_co_u32_e64 v182, s[30:31], 0, v182, s[26:27]
	v_cmp_eq_u32_e64 s[26:27], v250, v181
	v_cmp_lt_u32_e64 s[28:29], s41, v0
	s_and_b64 s[26:27], s[26:27], s[28:29]
	s_add_i32 s41, s41, 1
	v_addc_co_u32_e64 v182, s[30:31], 0, v182, s[26:27]
	v_cmp_eq_u32_e64 s[26:27], v251, v181
	v_cmp_lt_u32_e64 s[28:29], s41, v0
	s_and_b64 s[26:27], s[26:27], s[28:29]
	s_add_i32 s41, s41, 1
	v_addc_co_u32_e64 v182, s[30:31], 0, v182, s[26:27]
	v_lshlrev_b32_e32 v183, 2, v181
	ds_read_b32 v183, v183 offset:4096
	s_waitcnt lgkmcnt(0)
	v_add_u32_e32 v4, v183, v182
	v_lshl_add_u64 v[2:3], s[20:21], 0, v[2:3]
	v_or_b32_e32 v7, s40, v148
	s_waitcnt lgkmcnt(0)
	v_ashrrev_i32_e32 v5, 31, v4
	global_store_dword v[2:3], v4, off
	v_lshlrev_b64 v[2:3], 2, v[4:5]
	v_lshl_add_u64 v[4:5], s[18:19], 0, v[2:3]
	v_lshl_add_u64 v[2:3], s[22:23], 0, v[2:3]
	s_waitcnt vmcnt(1)
	global_store_dword v[4:5], v6, off
	global_store_dword v[2:3], v7, off
